# c40: c37 + ROUTE phase: the router-gain table fill issues all 32 loads up front (one memory round trip instead of four)
# speedup vs baseline: 1.0099x; 1.0038x over previous
; __global__ void __launch_bounds__(NTHREADS, 2) fwd(Args args) {
;     ...
;         { const float* gain = norm_ffn_ + DM;
;           for (int idx = F.tid; idx < 8192; idx += NTHREADS) { const int k = idx >> 3; grt[(idx & 7) * 1024 + ((k >> 2) & 3) * 256 + (k >> 4) * 4 + (k & 3)] = args.in[17][idx] * gain[k]; } }
;         if (F.tid < MOE_MAX_SLOTS / GRID) SDEST[F.bid * (MOE_MAX_SLOTS / GRID) + F.tid] = -1;
.LBB0_1098:
	v_mov_b32_e32 v4, v2
	v_lshrrev_b32_e32 v1, 1, v2
	v_lshrrev_b32_e32 v12, 1, v3
	v_add_u32_e32 v8, 0x400, v3
	v_mov_b32_e32 v9, v5
	v_lshl_add_u64 v[10:11], v[4:5], 2, s[54:55]
	v_mov_b32_e32 v4, v3
	v_and_b32_e32 v1, 0x7ffffffc, v1
	v_and_b32_e32 v18, 0x7ffffffc, v12
	v_lshl_add_u64 v[12:13], v[8:9], 2, s[54:55]
	v_lshrrev_b32_e32 v9, 1, v8
	v_lshl_add_u64 v[14:15], v[4:5], 2, s[54:55]
	v_add_u32_e32 v4, 0x400, v2
	global_load_dword v200, v1, s[8:9]
	global_load_dword v201, v18, s[8:9]
	v_and_b32_e32 v1, 0x7ffffffc, v9
	v_lshrrev_b32_e32 v9, 1, v4
	global_load_dword v202, v[10:11], off
	global_load_dword v203, v[14:15], off
	v_lshl_add_u64 v[10:11], v[4:5], 2, s[54:55]
	v_and_b32_e32 v9, 0x7ffffffc, v9
	global_load_dword v204, v[10:11], off
	global_load_dword v205, v[12:13], off
	s_nop 0
	global_load_dword v206, v9, s[8:9]
	global_load_dword v207, v1, s[8:9]
	v_add_u32_e32 v3, 0x800, v3
	v_add_u32_e32 v2, 0x800, v2
	v_mov_b32_e32 v4, v2
	v_lshrrev_b32_e32 v1, 1, v2
	v_lshrrev_b32_e32 v12, 1, v3
	v_add_u32_e32 v8, 0x400, v3
	v_mov_b32_e32 v9, v5
	v_lshl_add_u64 v[10:11], v[4:5], 2, s[54:55]
	v_mov_b32_e32 v4, v3
	v_and_b32_e32 v1, 0x7ffffffc, v1
	v_and_b32_e32 v18, 0x7ffffffc, v12
	v_lshl_add_u64 v[12:13], v[8:9], 2, s[54:55]
	v_lshrrev_b32_e32 v9, 1, v8
	v_lshl_add_u64 v[14:15], v[4:5], 2, s[54:55]
	v_add_u32_e32 v4, 0x400, v2
	global_load_dword v208, v1, s[8:9]
	global_load_dword v209, v18, s[8:9]
	v_and_b32_e32 v1, 0x7ffffffc, v9
	v_lshrrev_b32_e32 v9, 1, v4
	global_load_dword v210, v[10:11], off
	global_load_dword v211, v[14:15], off
	v_lshl_add_u64 v[10:11], v[4:5], 2, s[54:55]
	v_and_b32_e32 v9, 0x7ffffffc, v9
	global_load_dword v212, v[10:11], off
	global_load_dword v213, v[12:13], off
	s_nop 0
	global_load_dword v214, v9, s[8:9]
	global_load_dword v215, v1, s[8:9]
	v_add_u32_e32 v3, 0x800, v3
	v_add_u32_e32 v2, 0x800, v2
	v_mov_b32_e32 v4, v2
	v_lshrrev_b32_e32 v1, 1, v2
	v_lshrrev_b32_e32 v12, 1, v3
	v_add_u32_e32 v8, 0x400, v3
	v_mov_b32_e32 v9, v5
	v_lshl_add_u64 v[10:11], v[4:5], 2, s[54:55]
	v_mov_b32_e32 v4, v3
	v_and_b32_e32 v1, 0x7ffffffc, v1
	v_and_b32_e32 v18, 0x7ffffffc, v12
	v_lshl_add_u64 v[12:13], v[8:9], 2, s[54:55]
	v_lshrrev_b32_e32 v9, 1, v8
	v_lshl_add_u64 v[14:15], v[4:5], 2, s[54:55]
	v_add_u32_e32 v4, 0x400, v2
	global_load_dword v216, v1, s[8:9]
	global_load_dword v217, v18, s[8:9]
	v_and_b32_e32 v1, 0x7ffffffc, v9
	v_lshrrev_b32_e32 v9, 1, v4
	global_load_dword v218, v[10:11], off
	global_load_dword v219, v[14:15], off
	v_lshl_add_u64 v[10:11], v[4:5], 2, s[54:55]
	v_and_b32_e32 v9, 0x7ffffffc, v9
	global_load_dword v220, v[10:11], off
	global_load_dword v221, v[12:13], off
	s_nop 0
	global_load_dword v222, v9, s[8:9]
	global_load_dword v223, v1, s[8:9]
	v_add_u32_e32 v3, 0x800, v3
	v_add_u32_e32 v2, 0x800, v2
	v_mov_b32_e32 v4, v2
	v_lshrrev_b32_e32 v1, 1, v2
	v_lshrrev_b32_e32 v12, 1, v3
	v_add_u32_e32 v8, 0x400, v3
	v_mov_b32_e32 v9, v5
	v_lshl_add_u64 v[10:11], v[4:5], 2, s[54:55]
	v_mov_b32_e32 v4, v3
	v_and_b32_e32 v1, 0x7ffffffc, v1
	v_and_b32_e32 v18, 0x7ffffffc, v12
	v_lshl_add_u64 v[12:13], v[8:9], 2, s[54:55]
	v_lshrrev_b32_e32 v9, 1, v8
	v_lshl_add_u64 v[14:15], v[4:5], 2, s[54:55]
	v_add_u32_e32 v4, 0x400, v2
	global_load_dword v224, v1, s[8:9]
	global_load_dword v225, v18, s[8:9]
	v_and_b32_e32 v1, 0x7ffffffc, v9
	v_lshrrev_b32_e32 v9, 1, v4
	global_load_dword v226, v[10:11], off
	global_load_dword v227, v[14:15], off
	v_lshl_add_u64 v[10:11], v[4:5], 2, s[54:55]
	v_and_b32_e32 v9, 0x7ffffffc, v9
	global_load_dword v228, v[10:11], off
	global_load_dword v229, v[12:13], off
	s_nop 0
	global_load_dword v230, v9, s[8:9]
	global_load_dword v231, v1, s[8:9]
	v_add_u32_e32 v3, 0xffffe800, v3
	v_add_u32_e32 v2, 0xffffe800, v2
	v_add_u32_e32 v8, 0x400, v3
	v_add_u32_e32 v4, 0x400, v2
	v_lshlrev_b32_e32 v1, 10, v3
	v_lshlrev_b32_e32 v9, 10, v2
	v_lshlrev_b32_e32 v12, 3, v3
	v_lshlrev_b32_e32 v13, 3, v2
	v_lshrrev_b32_e32 v21, 5, v2
	v_and_b32_e32 v1, 0x1c00, v1
	v_and_b32_e32 v9, 0x1c00, v9
	v_and_b32_e32 v12, 0x300, v12
	v_and_b32_e32 v13, 0x300, v13
	v_and_b32_e32 v21, 0xfc, v21
	v_lshlrev_b32_e32 v22, 10, v8
	v_lshlrev_b32_e32 v23, 3, v8
	v_lshlrev_b32_e32 v9, 2, v9
	v_lshlrev_b32_e32 v1, 2, v1
	v_lshlrev_b32_e32 v13, 2, v13
	v_lshlrev_b32_e32 v12, 2, v12
	v_lshrrev_b32_e32 v8, 5, v8
	v_lshlrev_b32_e32 v21, 2, v21
	v_and_b32_e32 v22, 0x1c00, v22
	v_and_b32_e32 v23, 0x300, v23
	v_add3_u32 v9, 0, v9, v13
	v_add3_u32 v1, 0, v1, v12
	v_lshlrev_b32_e32 v12, 10, v4
	v_lshlrev_b32_e32 v13, 3, v4
	v_and_b32_e32 v8, 0xfc, v8
	v_lshrrev_b32_e32 v4, 5, v4
	v_lshlrev_b32_e32 v22, 2, v22
	v_lshlrev_b32_e32 v23, 2, v23
	v_add3_u32 v21, v9, v21, v6
	v_and_b32_e32 v9, 0x1c00, v12
	v_and_b32_e32 v12, 0x300, v13
	v_lshrrev_b32_e32 v20, 5, v3
	v_lshlrev_b32_e32 v8, 2, v8
	v_and_b32_e32 v4, 0xfc, v4
	v_add3_u32 v13, 0, v22, v23
	v_lshlrev_b32_e32 v9, 2, v9
	v_lshlrev_b32_e32 v12, 2, v12
	v_add_u32_e32 v7, -2, v7
	v_and_b32_e32 v20, 0xfc, v20
	v_lshlrev_b32_e32 v4, 2, v4
	v_add3_u32 v13, v13, v8, v6
	v_add3_u32 v8, 0, v9, v12
	v_cmp_eq_u32_e32 vcc, 0, v7
	v_lshlrev_b32_e32 v20, 2, v20
	v_add3_u32 v4, v8, v4, v6
	v_add_u32_e32 v3, 0x800, v3
	v_add_u32_e32 v2, 0x800, v2
	s_or_b64 s[12:13], vcc, s[12:13]
	v_add3_u32 v1, v1, v20, v6
	s_waitcnt vmcnt(28)
	v_pk_mul_f32 v[8:9], v[202:203], v[200:201]
	ds_write_b32 v21, v8
	ds_write_b32 v1, v9
	s_waitcnt vmcnt(24)
; __global__ void __launch_bounds__(NTHREADS, 2) fwd(Args args) {
;     ...
;         { const float* gain = norm_ffn_ + DM;
;           for (int idx = F.tid; idx < 8192; idx += NTHREADS) { const int k = idx >> 3; grt[(idx & 7) * 1024 + ((k >> 2) & 3) * 256 + (k >> 4) * 4 + (k & 3)] = args.in[17][idx] * gain[k]; } }
;         if (F.tid < MOE_MAX_SLOTS / GRID) SDEST[F.bid * (MOE_MAX_SLOTS / GRID) + F.tid] = -1;
	v_pk_mul_f32 v[8:9], v[204:205], v[206:207]
	ds_write_b32 v4, v8
	ds_write_b32 v13, v9
	v_add_u32_e32 v8, 0x400, v3
	v_add_u32_e32 v4, 0x400, v2
	v_lshlrev_b32_e32 v1, 10, v3
	v_lshlrev_b32_e32 v9, 10, v2
	v_lshlrev_b32_e32 v12, 3, v3
	v_lshlrev_b32_e32 v13, 3, v2
	v_lshrrev_b32_e32 v21, 5, v2
	v_and_b32_e32 v1, 0x1c00, v1
	v_and_b32_e32 v9, 0x1c00, v9
	v_and_b32_e32 v12, 0x300, v12
	v_and_b32_e32 v13, 0x300, v13
	v_and_b32_e32 v21, 0xfc, v21
	v_lshlrev_b32_e32 v22, 10, v8
	v_lshlrev_b32_e32 v23, 3, v8
	v_lshlrev_b32_e32 v9, 2, v9
	v_lshlrev_b32_e32 v1, 2, v1
	v_lshlrev_b32_e32 v13, 2, v13
	v_lshlrev_b32_e32 v12, 2, v12
	v_lshrrev_b32_e32 v8, 5, v8
	v_lshlrev_b32_e32 v21, 2, v21
	v_and_b32_e32 v22, 0x1c00, v22
	v_and_b32_e32 v23, 0x300, v23
	v_add3_u32 v9, 0, v9, v13
	v_add3_u32 v1, 0, v1, v12
	v_lshlrev_b32_e32 v12, 10, v4
	v_lshlrev_b32_e32 v13, 3, v4
	v_and_b32_e32 v8, 0xfc, v8
	v_lshrrev_b32_e32 v4, 5, v4
	v_lshlrev_b32_e32 v22, 2, v22
	v_lshlrev_b32_e32 v23, 2, v23
	v_add3_u32 v21, v9, v21, v6
	v_and_b32_e32 v9, 0x1c00, v12
	v_and_b32_e32 v12, 0x300, v13
	v_lshrrev_b32_e32 v20, 5, v3
	v_lshlrev_b32_e32 v8, 2, v8
	v_and_b32_e32 v4, 0xfc, v4
	v_add3_u32 v13, 0, v22, v23
	v_lshlrev_b32_e32 v9, 2, v9
	v_lshlrev_b32_e32 v12, 2, v12
	v_add_u32_e32 v7, -2, v7
	v_and_b32_e32 v20, 0xfc, v20
	v_lshlrev_b32_e32 v4, 2, v4
	v_add3_u32 v13, v13, v8, v6
	v_add3_u32 v8, 0, v9, v12
	v_cmp_eq_u32_e32 vcc, 0, v7
	v_lshlrev_b32_e32 v20, 2, v20
	v_add3_u32 v4, v8, v4, v6
	v_add_u32_e32 v3, 0x800, v3
	v_add_u32_e32 v2, 0x800, v2
	s_or_b64 s[12:13], vcc, s[12:13]
	v_add3_u32 v1, v1, v20, v6
	s_waitcnt vmcnt(20)
	v_pk_mul_f32 v[8:9], v[210:211], v[208:209]
	ds_write_b32 v21, v8
	ds_write_b32 v1, v9
	s_waitcnt vmcnt(16)
	v_pk_mul_f32 v[8:9], v[212:213], v[214:215]
	ds_write_b32 v4, v8
	ds_write_b32 v13, v9
	v_add_u32_e32 v8, 0x400, v3
	v_add_u32_e32 v4, 0x400, v2
	v_lshlrev_b32_e32 v1, 10, v3
	v_lshlrev_b32_e32 v9, 10, v2
	v_lshlrev_b32_e32 v12, 3, v3
	v_lshlrev_b32_e32 v13, 3, v2
	v_lshrrev_b32_e32 v21, 5, v2
	v_and_b32_e32 v1, 0x1c00, v1
	v_and_b32_e32 v9, 0x1c00, v9
	v_and_b32_e32 v12, 0x300, v12
	v_and_b32_e32 v13, 0x300, v13
	v_and_b32_e32 v21, 0xfc, v21
	v_lshlrev_b32_e32 v22, 10, v8
	v_lshlrev_b32_e32 v23, 3, v8
	v_lshlrev_b32_e32 v9, 2, v9
	v_lshlrev_b32_e32 v1, 2, v1
	v_lshlrev_b32_e32 v13, 2, v13
	v_lshlrev_b32_e32 v12, 2, v12
	v_lshrrev_b32_e32 v8, 5, v8
	v_lshlrev_b32_e32 v21, 2, v21
	v_and_b32_e32 v22, 0x1c00, v22
	v_and_b32_e32 v23, 0x300, v23
	v_add3_u32 v9, 0, v9, v13
	v_add3_u32 v1, 0, v1, v12
	v_lshlrev_b32_e32 v12, 10, v4
	v_lshlrev_b32_e32 v13, 3, v4
	v_and_b32_e32 v8, 0xfc, v8
	v_lshrrev_b32_e32 v4, 5, v4
	v_lshlrev_b32_e32 v22, 2, v22
	v_lshlrev_b32_e32 v23, 2, v23
	v_add3_u32 v21, v9, v21, v6
	v_and_b32_e32 v9, 0x1c00, v12
	v_and_b32_e32 v12, 0x300, v13
	v_lshrrev_b32_e32 v20, 5, v3
	v_lshlrev_b32_e32 v8, 2, v8
	v_and_b32_e32 v4, 0xfc, v4
	v_add3_u32 v13, 0, v22, v23
	v_lshlrev_b32_e32 v9, 2, v9
	v_lshlrev_b32_e32 v12, 2, v12
	v_add_u32_e32 v7, -2, v7
	v_and_b32_e32 v20, 0xfc, v20
	v_lshlrev_b32_e32 v4, 2, v4
	v_add3_u32 v13, v13, v8, v6
	v_add3_u32 v8, 0, v9, v12
	v_cmp_eq_u32_e32 vcc, 0, v7
	v_lshlrev_b32_e32 v20, 2, v20
	v_add3_u32 v4, v8, v4, v6
	v_add_u32_e32 v3, 0x800, v3
	v_add_u32_e32 v2, 0x800, v2
	s_or_b64 s[12:13], vcc, s[12:13]
	v_add3_u32 v1, v1, v20, v6
	s_waitcnt vmcnt(12)
	v_pk_mul_f32 v[8:9], v[218:219], v[216:217]
	ds_write_b32 v21, v8
	ds_write_b32 v1, v9
	s_waitcnt vmcnt(8)
	v_pk_mul_f32 v[8:9], v[220:221], v[222:223]
	ds_write_b32 v4, v8
	ds_write_b32 v13, v9
	v_add_u32_e32 v8, 0x400, v3
	v_add_u32_e32 v4, 0x400, v2
	v_lshlrev_b32_e32 v1, 10, v3
	v_lshlrev_b32_e32 v9, 10, v2
	v_lshlrev_b32_e32 v12, 3, v3
	v_lshlrev_b32_e32 v13, 3, v2
	v_lshrrev_b32_e32 v21, 5, v2
	v_and_b32_e32 v1, 0x1c00, v1
	v_and_b32_e32 v9, 0x1c00, v9
	v_and_b32_e32 v12, 0x300, v12
	v_and_b32_e32 v13, 0x300, v13
	v_and_b32_e32 v21, 0xfc, v21
	v_lshlrev_b32_e32 v22, 10, v8
	v_lshlrev_b32_e32 v23, 3, v8
	v_lshlrev_b32_e32 v9, 2, v9
	v_lshlrev_b32_e32 v1, 2, v1
	v_lshlrev_b32_e32 v13, 2, v13
	v_lshlrev_b32_e32 v12, 2, v12
	v_lshrrev_b32_e32 v8, 5, v8
	v_lshlrev_b32_e32 v21, 2, v21
	v_and_b32_e32 v22, 0x1c00, v22
	v_and_b32_e32 v23, 0x300, v23
	v_add3_u32 v9, 0, v9, v13
	v_add3_u32 v1, 0, v1, v12
	v_lshlrev_b32_e32 v12, 10, v4
	v_lshlrev_b32_e32 v13, 3, v4
	v_and_b32_e32 v8, 0xfc, v8
	v_lshrrev_b32_e32 v4, 5, v4
	v_lshlrev_b32_e32 v22, 2, v22
	v_lshlrev_b32_e32 v23, 2, v23
	v_add3_u32 v21, v9, v21, v6
	v_and_b32_e32 v9, 0x1c00, v12
	v_and_b32_e32 v12, 0x300, v13
	v_lshrrev_b32_e32 v20, 5, v3
	v_lshlrev_b32_e32 v8, 2, v8
	v_and_b32_e32 v4, 0xfc, v4
	v_add3_u32 v13, 0, v22, v23
	v_lshlrev_b32_e32 v9, 2, v9
	v_lshlrev_b32_e32 v12, 2, v12
	v_add_u32_e32 v7, -2, v7
	v_and_b32_e32 v20, 0xfc, v20
	v_lshlrev_b32_e32 v4, 2, v4
	v_add3_u32 v13, v13, v8, v6
	v_add3_u32 v8, 0, v9, v12
	v_cmp_eq_u32_e32 vcc, 0, v7
	v_lshlrev_b32_e32 v20, 2, v20
	v_add3_u32 v4, v8, v4, v6
	v_add_u32_e32 v3, 0x800, v3
	v_add_u32_e32 v2, 0x800, v2
	s_or_b64 s[12:13], vcc, s[12:13]
	v_add3_u32 v1, v1, v20, v6
	s_waitcnt vmcnt(4)
	v_pk_mul_f32 v[8:9], v[226:227], v[224:225]
	ds_write_b32 v21, v8
	ds_write_b32 v1, v9
	s_waitcnt vmcnt(0)
	v_pk_mul_f32 v[8:9], v[228:229], v[230:231]
	ds_write_b32 v4, v8
	ds_write_b32 v13, v9
	s_mov_b64 s[12:13], exec
	s_or_b64 exec, exec, s[12:13]
	v_cmp_eq_u32_e64 s[4:5], 2, 0
	s_and_saveexec_b64 s[12:13], s[4:5]
	s_cbranch_execz .LBB0_1101
	v_mov_b32_e32 v5, 0
	v_mov_b32_e32 v4, v2
	v_lshrrev_b32_e32 v1, 1, v2
	v_lshl_add_u64 v[8:9], v[4:5], 2, s[54:55]
	v_mov_b32_e32 v4, v3
	v_and_b32_e32 v1, 0x7ffffffc, v1
	v_lshrrev_b32_e32 v7, 1, v3
	v_lshl_add_u64 v[4:5], v[4:5], 2, s[54:55]
	v_and_b32_e32 v7, 0x7ffffffc, v7
	global_load_dword v10, v1, s[8:9]
	global_load_dword v11, v7, s[8:9]
	global_load_dword v12, v[8:9], off
	global_load_dword v13, v[4:5], off
	v_lshlrev_b32_e32 v1, 10, v3
	v_lshlrev_b32_e32 v4, 10, v2
	v_lshlrev_b32_e32 v5, 3, v3
	v_lshlrev_b32_e32 v7, 3, v2
	v_lshrrev_b32_e32 v3, 5, v3
	v_lshrrev_b32_e32 v2, 5, v2
	v_and_b32_e32 v1, 0x1c00, v1
	v_and_b32_e32 v4, 0x1c00, v4
	v_and_b32_e32 v5, 0x300, v5
	v_and_b32_e32 v7, 0x300, v7
	v_and_b32_e32 v3, 0xfc, v3
	v_and_b32_e32 v2, 0xfc, v2
	v_lshlrev_b32_e32 v4, 2, v4
	v_lshlrev_b32_e32 v1, 2, v1
	v_lshlrev_b32_e32 v7, 2, v7
	v_lshlrev_b32_e32 v5, 2, v5
	v_lshlrev_b32_e32 v2, 2, v2
	v_lshlrev_b32_e32 v3, 2, v3
	v_add3_u32 v4, 0, v4, v7
	v_add3_u32 v1, 0, v1, v5
	v_add3_u32 v4, v4, v2, v6
	v_add3_u32 v1, v1, v3, v6
	s_waitcnt vmcnt(0)
	v_pk_mul_f32 v[2:3], v[12:13], v[10:11]
	ds_write_b32 v4, v2
	ds_write_b32 v1, v3
